# speedup vs baseline: 1.0053x; 1.0012x over previous
_Z11lstm_kernelPKiPKhPKfS4_S4_Pf:
	s_load_dwordx4 s[12:15], s[0:1], 0x0
	v_readfirstlane_b32 s19, v0
	v_or_b32_e32 v3, 0x400, v0
	s_movk_i32 s4, 0x500
	s_lshr_b32 s7, s19, 6
	s_lshl_b32 s18, s2, 6
	s_mulk_i32 s2, 0x1400
	v_mov_b32_e32 v2, 0x4ff
	v_cmp_gt_u32_e32 vcc, s4, v3
	s_mul_hi_i32 s3, s18, 0x50
	s_waitcnt lgkmcnt(0)
	s_add_u32 s2, s12, s2
	v_cndmask_b32_e32 v2, v2, v3, vcc
	s_addc_u32 s3, s13, s3
	v_lshlrev_b32_e32 v1, 2, v0
	v_lshlrev_b32_e32 v4, 2, v2
	s_movk_i32 s4, 0x184
	v_or_b32_e32 v28, 0x200, v0
	global_load_dword v29, v1, s[2:3]
	global_load_dword v30, v1, s[2:3] offset:2048
	global_load_dword v2, v4, s[2:3]
	v_mov_b32_e32 v4, 0x383
	v_cmp_gt_u32_e32 vcc, s4, v0
	s_add_u32 s2, s14, 0x34000
	s_addc_u32 s3, s15, 0
	v_cndmask_b32_e32 v4, v4, v28, vcc
	v_lshlrev_b32_e32 v31, 4, v0
	v_lshlrev_b32_e32 v4, 4, v4
	global_load_dwordx4 v[6:9], v31, s[2:3]
	global_load_dwordx4 v[10:13], v4, s[2:3]
	v_and_b32_e32 v4, 0x7f, v0
	v_lshlrev_b32_e32 v18, 4, v4
	v_mov_b32_e32 v19, 0
	v_lshl_add_u64 v[4:5], s[14:15], 0, v[18:19]
	s_mov_b32 s2, 0x37000
	v_add_co_u32_e64 v4, s[2:3], s2, v4
	s_nop 1
	v_addc_co_u32_e64 v5, s[2:3], 0, v5, s[2:3]
	global_load_dwordx4 v[14:17], v[4:5], off offset:2112
	s_movk_i32 s22, 0x410
	s_movk_i32 s2, 0x4ff
	v_and_b32_e32 v4, 63, v0
	v_cmp_lt_u32_e64 s[2:3], s2, v3
	s_mul_i32 s5, s7, 0x6000
	s_mul_hi_u32 s4, s7, 0x6000
	s_add_u32 s8, s14, s5
	s_addc_u32 s9, s15, s4
	v_lshlrev_b32_e32 v210, 4, v4
	v_mov_b32_e32 v211, v19
	v_lshl_add_u64 v[20:21], s[8:9], 0, v[210:211]
	s_movk_i32 s4, 0x2000
	v_add_co_u32_e64 v22, s[4:5], s4, v20
	s_nop 1
	v_addc_co_u32_e64 v23, s[4:5], 0, v21, s[4:5]
	s_movk_i32 s4, 0x3000
	s_nop 0
	v_add_co_u32_e64 v24, s[4:5], s4, v20
	global_load_dwordx4 v[90:93], v[22:23], off offset:1024
	global_load_dwordx4 v[86:89], v[22:23], off offset:2048
	v_addc_co_u32_e64 v25, s[4:5], 0, v21, s[4:5]
	s_movk_i32 s4, 0x5000
	s_nop 0
	v_add_co_u32_e64 v26, s[4:5], s4, v20
	s_nop 1
	v_addc_co_u32_e64 v27, s[4:5], 0, v21, s[4:5]
	global_load_dwordx4 v[82:85], v[22:23], off offset:3072
	global_load_dwordx4 v[46:49], v[26:27], off
	global_load_dwordx4 v[42:45], v[26:27], off offset:1024
	global_load_dwordx4 v[38:41], v[26:27], off offset:2048
	global_load_dwordx4 v[94:97], v[24:25], off offset:-4096
	global_load_dwordx4 v[34:37], v[26:27], off offset:3072
	s_movk_i32 s4, 0x1000
	v_add_co_u32_e64 v22, s[4:5], s4, v20
	global_load_dwordx4 v[126:129], v210, s[8:9]
	global_load_dwordx4 v[122:125], v210, s[8:9] offset:1024
	global_load_dwordx4 v[118:121], v210, s[8:9] offset:2048
	global_load_dwordx4 v[114:117], v210, s[8:9] offset:3072
	v_addc_co_u32_e64 v23, s[4:5], 0, v21, s[4:5]
	global_load_dwordx4 v[110:113], v[22:23], off
	global_load_dwordx4 v[106:109], v[22:23], off offset:1024
	global_load_dwordx4 v[102:105], v[22:23], off offset:2048
	global_load_dwordx4 v[98:101], v[22:23], off offset:3072
	global_load_dwordx4 v[78:81], v[24:25], off
	global_load_dwordx4 v[74:77], v[24:25], off offset:1024
	global_load_dwordx4 v[70:73], v[24:25], off offset:2048
	global_load_dwordx4 v[66:69], v[24:25], off offset:3072
	s_movk_i32 s4, 0x4000
	v_add_co_u32_e64 v20, s[4:5], s4, v20
	v_mov_b32_e32 v5, 0x4000
	s_nop 0
	v_addc_co_u32_e64 v21, s[4:5], 0, v21, s[4:5]
	global_load_dwordx4 v[62:65], v[20:21], off
	global_load_dwordx4 v[58:61], v[20:21], off offset:1024
	global_load_dwordx4 v[54:57], v[20:21], off offset:2048
	global_load_dwordx4 v[50:53], v[20:21], off offset:3072
	s_waitcnt vmcnt(26)
	ds_write_b128 v31, v[6:9] offset:16384
	v_lshl_or_b32 v5, v28, 4, v5
	v_add_u32_e32 v6, 0x9840, v31
	v_cndmask_b32_e32 v5, v6, v5, vcc
	s_waitcnt vmcnt(25)
	ds_write_b128 v5, v[10:13]
	s_waitcnt vmcnt(24)
	ds_write_b128 v18, v[14:17] offset:36928
	v_mul_u32_u24_e32 v5, 0xccd, v0
	v_lshrrev_b32_e32 v5, 16, v5
	s_mov_b32 s5, 0xffffec
	v_mul_u32_u24_e32 v6, 0xccd, v28
	s_movk_i32 s4, 0x90
	v_mad_u32_u24 v8, v5, s5, v0
	v_lshlrev_b32_e32 v5, 2, v5
	v_lshrrev_b32_e32 v6, 16, v6
	v_mul_lo_u32 v7, v29, s4
	v_lshl_or_b32 v5, v8, 8, v5
	ds_write_b32 v5, v7 offset:30784
	v_mul_lo_u32 v196, v29, s22
	v_add_u32_e32 v197, 0x24e80, v5
	ds_write_b32 v197, v196
	v_mad_u32_u24 v7, v6, s5, v28
	v_lshlrev_b32_e32 v6, 2, v6
	v_mul_lo_u32 v5, v30, s4
	v_lshl_or_b32 v6, v7, 8, v6
	ds_write_b32 v6, v5 offset:30784
	v_mul_lo_u32 v198, v30, s22
	v_add_u32_e32 v199, 0x24e80, v6
	ds_write_b32 v199, v198
	s_and_saveexec_b64 s[4:5], s[2:3]
	s_xor_b64 s[2:3], exec, s[4:5]
	v_mov_b32_e32 v3, 0x9840
	v_lshl_add_u32 v5, v0, 2, v3
	s_andn2_saveexec_b64 s[2:3], s[2:3]
	v_mul_u32_u24_e32 v5, 0xccd, v3
	s_mov_b32 s4, 0xffffec
	v_mul_u32_u24_sdwa v6, v5, s4 dst_sel:DWORD dst_unused:UNUSED_PAD src0_sel:WORD_1 src1_sel:DWORD
	v_add_lshl_u32 v3, v6, v3, 8
	v_mov_b32_e32 v6, 2
	v_lshlrev_b32_sdwa v5, v6, v5 dst_sel:DWORD dst_unused:UNUSED_PAD src0_sel:DWORD src1_sel:WORD_1
	s_movk_i32 s4, 0x7840
	v_add3_u32 v5, v5, v3, s4
	s_or_b64 exec, exec, s[2:3]
	v_lshrrev_b32_e32 v3, 5, v4
	s_movk_i32 s2, 0x90
	s_lshl_b32 s6, s7, 10
	s_mulk_i32 s7, 0xfd00
	v_and_b32_e32 v182, 31, v0
	v_mul_lo_u32 v200, v2, s22
	v_mul_lo_u32 v2, v2, s2
	s_add_i32 s7, s6, s7
	v_lshlrev_b32_e32 v229, 6, v3
	ds_write_b32 v5, v2
	v_add_u32_e32 v201, 0x1d640, v5
	ds_write_b32 v201, v200
	v_lshlrev_b32_e32 v230, 4, v3
	v_lshlrev_b32_e32 v228, 2, v182
	v_or_b32_e32 v2, s7, v229
	s_waitcnt lgkmcnt(0)
	s_barrier
	s_cmpk_lt_u32 s19, 0x100
	s_cbranch_scc1 .Llight_path
	s_setprio 1
	s_mov_b32 s12, 0xbeb17218
	v_add_u32_e32 v3, 0x7800, v228
	ds_read2_b32 v[138:139], v3 offset0:16 offset1:48
	ds_read_b128 v[18:21], v2 offset:36928
	ds_read_b128 v[22:25], v2 offset:36944
	s_waitcnt lgkmcnt(2)
	v_add_u32_e32 v3, v230, v138
	ds_read_b128 v[26:29], v2 offset:36960
	ds_read_b128 v[30:33], v2 offset:36976
	ds_read_b128 v[142:145], v3 offset:16384
	ds_read_b128 v[130:133], v3 offset:16416
	ds_read_b128 v[154:157], v3 offset:16448
	ds_read_b128 v[134:137], v3 offset:16480
	ds_read_b128 v[248:251], v2 offset:37104
	ds_read_b128 v[244:247], v2 offset:37088
	ds_read_b128 v[240:243], v2 offset:37072
	ds_read_b128 v[236:239], v2 offset:37056
	s_waitcnt vmcnt(17) lgkmcnt(7)
	v_mfma_f32_32x32x16_bf16 v[18:33], v[94:97], v[142:145], v[18:33]
	s_waitcnt lgkmcnt(6)
	v_mfma_f32_32x32x16_bf16 v[18:33], v[90:93], v[130:133], v[18:33]
	s_waitcnt lgkmcnt(5)
	v_mfma_f32_32x32x16_bf16 v[18:33], v[86:89], v[154:157], v[18:33]
	s_waitcnt lgkmcnt(4)
	v_mfma_f32_32x32x16_bf16 v[18:33], v[82:85], v[134:137], v[18:33]
	s_cmpk_lt_u32 s19, 0x100
	s_cselect_b64 s[2:3], -1, 0
	ds_read_b32 v158, v228 offset:31040
	v_add_u32_e32 v159, v230, v139
	s_nop 2
	v_exp_f32_e32 v139, v20
	v_exp_f32_e32 v138, v24
	v_exp_f32_e32 v141, v28
	v_exp_f32_e32 v140, v32
	v_exp_f32_e32 v18, v18
	v_exp_f32_e32 v20, v22
	v_exp_f32_e32 v22, v26
	v_add_f32_e32 v24, 1.0, v138
	v_add_f32_e32 v26, 1.0, v141
	v_add_f32_e32 v19, 1.0, v139
	v_exp_f32_e32 v23, v30
	v_add_f32_e32 v27, 1.0, v140
	v_fmac_f32_e32 v24, v20, v24
	v_fmac_f32_e32 v26, v22, v26
	v_fmac_f32_e32 v19, v18, v19
	v_fmac_f32_e32 v27, v23, v27
	v_rcp_f32_e32 v18, v24
	v_rcp_f32_e32 v22, v27
	v_rcp_f32_e32 v19, v19
	v_rcp_f32_e32 v23, v26
	v_exp_f32_e32 v146, v21
	v_exp_f32_e32 v147, v25
	s_mov_b32 s8, 0xc038aa3b
	s_mov_b32 s4, 0x4038aa3b
	v_mov_b64_e32 v[160:161], s[8:9]
	v_exp_f32_e32 v148, v29
	v_exp_f32_e32 v149, v33
	v_pk_fma_f32 v[20:21], v[138:139], s[4:5], v[160:161] op_sel_hi:[1,0,0]
	s_nop 0
	v_pk_mul_f32 v[214:215], v[20:21], v[18:19]
	v_pk_fma_f32 v[18:19], v[140:141], s[4:5], v[160:161] op_sel_hi:[1,0,0]
	s_nop 0
	v_pk_mul_f32 v[212:213], v[18:19], v[22:23]
	v_add_u32_e32 v231, s7, v229
	ds_read_b128 v[18:21], v231 offset:36928
	ds_read_b128 v[22:25], v231 offset:36944
	ds_read_b128 v[26:29], v231 offset:36960
	ds_read_b128 v[30:33], v231 offset:36976
	s_waitcnt lgkmcnt(5)
	v_mfma_f32_32x32x16_bf16 v[2:17], v[46:49], v[142:145], v[236:251]
	ds_read_b128 v[138:141], v159 offset:16384
	v_add_f32_e32 v162, 1.0, v146
	v_exp_f32_e32 v163, v215
	v_exp_f32_e32 v164, v214
	v_exp_f32_e32 v165, v213
	v_exp_f32_e32 v166, v212
	v_add_f32_e32 v142, 1.0, v147
	v_add_f32_e32 v143, 1.0, v148
	v_add_f32_e32 v144, 1.0, v149
	v_mfma_f32_32x32x16_bf16 v[2:17], v[42:45], v[130:133], v[2:17]
	ds_read_b128 v[146:149], v159 offset:16416
	v_fmac_f32_e32 v162, v162, v163
	v_fmac_f32_e32 v142, v142, v164
	v_fmac_f32_e32 v143, v143, v165
	v_fmac_f32_e32 v144, v144, v166
	v_mfma_f32_32x32x16_bf16 v[2:17], v[38:41], v[154:157], v[2:17]
	ds_read_b128 v[150:153], v159 offset:16448
	v_rcp_f32_e32 v130, v162
	v_rcp_f32_e32 v131, v142
	v_rcp_f32_e32 v132, v143
	v_rcp_f32_e32 v133, v144
	s_waitcnt vmcnt(16)
	v_mfma_f32_32x32x16_bf16 v[2:17], v[34:37], v[134:137], v[2:17]
	ds_read_b128 v[178:181], v159 offset:16480
	v_fma_f32 v130, -v163, v130, v130
	v_fma_f32 v131, -v164, v131, v131
	v_fma_f32 v132, -v165, v132, v132
	v_fma_f32 v133, -v166, v133, v133
	v_add_u32_e32 v211, s6, v210
	v_cvt_pk_bf16_f32 v252, v130, v131
	v_cvt_pk_bf16_f32 v253, v132, v133
	s_nop 3
	v_exp_f32_e32 v131, v4
	v_exp_f32_e32 v130, v8
	v_exp_f32_e32 v133, v12
	v_exp_f32_e32 v132, v16
	v_exp_f32_e32 v2, v2
	v_exp_f32_e32 v4, v6
	v_exp_f32_e32 v6, v10
	v_exp_f32_e32 v7, v14
	v_add_f32_e32 v3, 1.0, v131
	v_add_f32_e32 v8, 1.0, v130
	v_add_f32_e32 v10, 1.0, v133
	v_add_f32_e32 v11, 1.0, v132
	v_fmac_f32_e32 v3, v2, v3
	v_fmac_f32_e32 v8, v4, v8
	v_fmac_f32_e32 v10, v6, v10
	v_fmac_f32_e32 v11, v7, v11
	v_rcp_f32_e32 v3, v3
	v_rcp_f32_e32 v2, v8
	v_rcp_f32_e32 v7, v10
	v_rcp_f32_e32 v6, v11
	v_exp_f32_e32 v134, v5
	v_exp_f32_e32 v135, v9
	v_pk_fma_f32 v[4:5], v[130:131], s[4:5], v[160:161] op_sel_hi:[1,0,0]
	v_exp_f32_e32 v130, v13
	v_pk_mul_f32 v[204:205], v[4:5], v[2:3]
	v_pk_fma_f32 v[2:3], v[132:133], s[4:5], v[160:161] op_sel_hi:[1,0,0]
	v_exp_f32_e32 v131, v17
	v_pk_mul_f32 v[202:203], v[2:3], v[6:7]
	s_waitcnt lgkmcnt(3)
	v_mfma_f32_32x32x16_bf16 v[18:33], v[94:97], v[138:141], v[18:33]
	v_add_f32_e32 v132, 1.0, v134
	v_exp_f32_e32 v133, v205
	v_add_f32_e32 v134, 1.0, v135
	v_exp_f32_e32 v135, v204
	v_exp_f32_e32 v136, v203
	v_exp_f32_e32 v137, v202
	v_add_f32_e32 v130, 1.0, v130
	v_add_f32_e32 v131, 1.0, v131
	s_waitcnt lgkmcnt(2)
	v_mfma_f32_32x32x16_bf16 v[18:33], v[90:93], v[146:149], v[18:33]
	v_fmac_f32_e32 v132, v132, v133
	v_fmac_f32_e32 v134, v134, v135
	v_fmac_f32_e32 v130, v130, v136
	v_fmac_f32_e32 v131, v131, v137
	s_waitcnt lgkmcnt(1)
	v_mfma_f32_32x32x16_bf16 v[18:33], v[86:89], v[150:153], v[18:33]
	v_rcp_f32_e32 v132, v132
	v_rcp_f32_e32 v134, v134
	v_rcp_f32_e32 v130, v130
	v_rcp_f32_e32 v131, v131
	s_waitcnt lgkmcnt(0)
	v_mfma_f32_32x32x16_bf16 v[18:33], v[82:85], v[178:181], v[18:33]
	v_fma_f32 v132, -v133, v132, v132
	v_fma_f32 v133, -v135, v134, v134
	v_fma_f32 v134, -v136, v130, v130
	v_fma_f32 v131, -v137, v131, v131
	v_cvt_pk_bf16_f32 v254, v132, v133
	v_cvt_pk_bf16_f32 v255, v134, v131
	ds_write_b128 v211, v[252:255] offset:0
	s_waitcnt lgkmcnt(0)
	s_barrier
	s_load_dwordx8 s[4:11], s[0:1], 0x10
	ds_read_b32 v229, v228 offset:31168
	ds_read_b128 v[174:177], v210
	v_add_u32_e32 v183, v230, v158
	ds_read_b128 v[170:173], v210 offset:1024
	v_exp_f32_e32 v131, v20
	v_exp_f32_e32 v130, v24
	v_exp_f32_e32 v133, v28
	v_exp_f32_e32 v132, v32
	ds_read_b128 v[166:169], v210 offset:2048
	v_exp_f32_e32 v18, v18
	v_exp_f32_e32 v20, v22
	v_exp_f32_e32 v22, v26
	v_exp_f32_e32 v23, v30
	v_fma_f32 v19, v131, s12, s12
	v_fma_f32 v24, v130, s12, s12
	v_fma_f32 v26, v133, s12, s12
	v_fma_f32 v27, v132, s12, s12
	ds_read_b128 v[162:165], v210 offset:3072
	v_fmac_f32_e32 v19, v18, v19
	v_fmac_f32_e32 v24, v20, v24
	v_fmac_f32_e32 v26, v22, v26
	v_fmac_f32_e32 v27, v23, v27
	ds_read_b128 v[158:161], v210 offset:4096
	v_rcp_f32_e32 v19, v19
	v_rcp_f32_e32 v18, v24
	v_rcp_f32_e32 v23, v26
	v_rcp_f32_e32 v22, v27
	ds_read_b128 v[154:157], v210 offset:5120
	v_exp_f32_e32 v186, v21
	v_exp_f32_e32 v187, v25
	ds_read_b128 v[142:145], v210 offset:6144
	s_mov_b32 s0, 0xc038aa3b
	v_exp_f32_e32 v188, v29
	v_pk_fma_f32 v[200:201], v[130:131], v[18:19], v[18:19] neg_lo:[1,0,0] neg_hi:[1,0,0]
	v_exp_f32_e32 v189, v33
	v_pk_fma_f32 v[198:199], v[132:133], v[22:23], v[22:23] neg_lo:[1,0,0] neg_hi:[1,0,0]
	ds_read_b128 v[130:133], v210 offset:7168
	ds_read_b128 v[18:21], v231 offset:36928
	ds_read_b128 v[22:25], v231 offset:36944
	ds_read_b128 v[26:29], v231 offset:36960
	ds_read_b128 v[30:33], v231 offset:36976
	v_mfma_f32_32x32x16_bf16 v[2:17], v[46:49], v[138:141], v[236:251]
	ds_read_b128 v[134:137], v183 offset:16384
	v_add_f32_e32 v186, 1.0, v186
	v_exp_f32_e32 v190, v201
	v_exp_f32_e32 v191, v200
	v_exp_f32_e32 v192, v199
	v_exp_f32_e32 v193, v198
	v_add_f32_e32 v187, 1.0, v187
	v_add_f32_e32 v188, 1.0, v188
	v_add_f32_e32 v189, 1.0, v189
	v_mfma_f32_32x32x16_bf16 v[2:17], v[42:45], v[146:149], v[2:17]
	ds_read_b128 v[138:141], v183 offset:16416
	v_fmac_f32_e32 v186, v186, v190
	v_fmac_f32_e32 v187, v187, v191
	v_fmac_f32_e32 v188, v188, v192
	v_fmac_f32_e32 v189, v189, v193
	v_mfma_f32_32x32x16_bf16 v[2:17], v[38:41], v[150:153], v[2:17]
	ds_read_b128 v[146:149], v183 offset:16448
	v_rcp_f32_e32 v186, v186
	v_rcp_f32_e32 v187, v187
	v_rcp_f32_e32 v188, v188
	v_rcp_f32_e32 v189, v189
	v_mfma_f32_32x32x16_bf16 v[2:17], v[34:37], v[178:181], v[2:17]
	ds_read_b128 v[150:153], v183 offset:16480
	v_fma_f32 v183, -v190, v186, v186
	v_fma_f32 v186, -v191, v187, v187
	v_fma_f32 v187, -v192, v188, v188
	v_fma_f32 v188, -v193, v189, v189
	s_waitcnt vmcnt(15) lgkmcnt(0)
	v_mfma_f32_32x32x16_bf16 v[18:33], v[126:129], v[174:177], v[18:33]
	v_cvt_pk_bf16_f32 v252, v183, v186
	v_cvt_pk_bf16_f32 v253, v187, v188
	s_waitcnt vmcnt(14)
	v_mfma_f32_32x32x16_bf16 v[18:33], v[122:125], v[170:173], v[18:33]
	s_nop 0
	v_exp_f32_e32 v179, v4
	v_exp_f32_e32 v178, v8
	v_exp_f32_e32 v181, v12
	v_exp_f32_e32 v180, v16
	s_waitcnt vmcnt(13)
	v_mfma_f32_32x32x16_bf16 v[18:33], v[118:121], v[166:169], v[18:33]
	v_exp_f32_e32 v2, v2
	v_exp_f32_e32 v4, v6
	v_exp_f32_e32 v7, v10
	v_exp_f32_e32 v8, v14
	v_fma_f32 v3, v179, s12, s12
	v_fma_f32 v6, v178, s12, s12
	v_fma_f32 v10, v181, s12, s12
	v_fma_f32 v11, v180, s12, s12
	s_waitcnt vmcnt(12)
	v_mfma_f32_32x32x16_bf16 v[18:33], v[114:117], v[162:165], v[18:33]
	v_fmac_f32_e32 v3, v2, v3
	v_fmac_f32_e32 v6, v4, v6
	v_fmac_f32_e32 v10, v7, v10
	v_fmac_f32_e32 v11, v8, v11
	s_waitcnt vmcnt(11)
	v_mfma_f32_32x32x16_bf16 v[18:33], v[110:113], v[158:161], v[18:33]
	v_rcp_f32_e32 v3, v3
	v_rcp_f32_e32 v2, v6
	v_rcp_f32_e32 v7, v10
	v_rcp_f32_e32 v6, v11
	s_waitcnt vmcnt(10)
	v_mfma_f32_32x32x16_bf16 v[18:33], v[106:109], v[154:157], v[18:33]
	v_exp_f32_e32 v183, v5
	v_exp_f32_e32 v186, v9
	s_waitcnt vmcnt(9)
	v_mfma_f32_32x32x16_bf16 v[18:33], v[102:105], v[142:145], v[18:33]
	v_pk_fma_f32 v[206:207], v[178:179], v[2:3], v[2:3] neg_lo:[1,0,0] neg_hi:[1,0,0]
	v_exp_f32_e32 v178, v13
	v_exp_f32_e32 v179, v17
	v_pk_fma_f32 v[208:209], v[180:181], v[6:7], v[6:7] neg_lo:[1,0,0] neg_hi:[1,0,0]
	s_waitcnt vmcnt(8)
	v_mfma_f32_32x32x16_bf16 v[18:33], v[98:101], v[130:133], v[18:33]
	v_mfma_f32_32x32x16_bf16 v[18:33], v[94:97], v[134:137], v[18:33]
	v_add_f32_e32 v180, 1.0, v183
	v_exp_f32_e32 v181, v207
	v_add_f32_e32 v183, 1.0, v186
	v_exp_f32_e32 v184, v206
	v_exp_f32_e32 v185, v209
	v_exp_f32_e32 v186, v208
	v_add_f32_e32 v178, 1.0, v178
	v_add_f32_e32 v179, 1.0, v179
	v_mfma_f32_32x32x16_bf16 v[18:33], v[90:93], v[138:141], v[18:33]
	v_fmac_f32_e32 v180, v180, v181
	v_fmac_f32_e32 v183, v183, v184
	v_fmac_f32_e32 v178, v178, v185
	v_fmac_f32_e32 v179, v179, v186
	v_mfma_f32_32x32x16_bf16 v[18:33], v[86:89], v[146:149], v[18:33]
	v_rcp_f32_e32 v180, v180
	v_rcp_f32_e32 v183, v183
	v_rcp_f32_e32 v178, v178
	v_rcp_f32_e32 v179, v179
	v_mfma_f32_32x32x16_bf16 v[18:33], v[82:85], v[150:153], v[18:33]
	v_fma_f32 v180, -v181, v180, v180
	v_fma_f32 v181, -v184, v183, v183
	v_fma_f32 v183, -v185, v178, v178
	v_fma_f32 v179, -v186, v179, v179
	v_cvt_pk_bf16_f32 v254, v180, v181
	v_cvt_pk_bf16_f32 v255, v183, v179
	ds_write_b128 v211, v[252:255] offset:8192
	s_waitcnt lgkmcnt(0)
	s_barrier
	v_mov_b32_e32 v178, 0x7a40
	v_lshl_add_u32 v232, v182, 2, v178
	s_mov_b32 s1, -1
	s_waitcnt vmcnt(0)
	s_branch .LBB1_14
.LBB1_13:
	v_mfma_f32_32x32x16_bf16 v[2:17], v[78:81], v[206:209], v[236:251]
	ds_read_b128 v[174:177], v210
	v_add_u32_e32 v195, v230, v228
	v_mfma_f32_32x32x16_bf16 v[2:17], v[74:77], v[190:193], v[2:17]
	ds_read_b128 v[170:173], v210 offset:1024
	v_exp_f32_e32 v199, v28
	v_exp_f32_e32 v198, v32
	v_exp_f32_e32 v197, v20
	v_exp_f32_e32 v196, v24
	v_mfma_f32_32x32x16_bf16 v[2:17], v[70:73], v[158:161], v[2:17]
	ds_read_b128 v[166:169], v210 offset:2048
	v_exp_f32_e32 v18, v18
	v_exp_f32_e32 v22, v22
	v_exp_f32_e32 v24, v26
	v_exp_f32_e32 v26, v30
	v_fma_f32 v20, v197, s12, s12
	v_fma_f32 v28, v196, s12, s12
	v_fma_f32 v30, v199, s12, s12
	v_fma_f32 v32, v198, s12, s12
	v_mfma_f32_32x32x16_bf16 v[2:17], v[66:69], v[142:145], v[2:17]
	ds_read_b128 v[162:165], v210 offset:3072
	v_exp_f32_e32 v19, v19
	v_exp_f32_e32 v23, v23
	v_exp_f32_e32 v27, v27
	v_exp_f32_e32 v31, v31
	v_fmac_f32_e32 v20, v18, v20
	v_fmac_f32_e32 v28, v22, v28
	v_fmac_f32_e32 v30, v24, v30
	v_fmac_f32_e32 v32, v26, v32
	v_mfma_f32_32x32x16_bf16 v[2:17], v[62:65], v[154:157], v[2:17]
	ds_read_b128 v[158:161], v210 offset:4096
	v_add_f32_e32 v22, 1.0, v19
	v_rcp_f32_e32 v19, v20
	v_rcp_f32_e32 v18, v28
	v_add_f32_e32 v20, 1.0, v23
	v_rcp_f32_e32 v191, v30
	v_rcp_f32_e32 v190, v32
	v_mfma_f32_32x32x16_bf16 v[2:17], v[58:61], v[182:185], v[2:17]
	ds_read_b128 v[154:157], v210 offset:5120
	v_exp_f32_e32 v206, v21
	v_exp_f32_e32 v207, v25
	v_add_f32_e32 v23, 1.0, v27
	v_rcp_f32_e32 v192, v20
	v_add_f32_e32 v20, 1.0, v31
	v_rcp_f32_e32 v193, v22
	v_mfma_f32_32x32x16_bf16 v[2:17], v[54:57], v[186:189], v[2:17]
	ds_read_b128 v[142:145], v210 offset:6144
	v_exp_f32_e32 v208, v29
	v_exp_f32_e32 v209, v33
	v_rcp_f32_e32 v183, v23
	v_rcp_f32_e32 v182, v20
	v_mfma_f32_32x32x16_bf16 v[2:17], v[50:53], v[134:137], v[2:17]
	ds_read_b128 v[130:133], v210 offset:7168
	v_fma_f32 v186, -v196, v18, v18
	v_fma_f32 v187, -v197, v19, v19
	ds_read_b128 v[18:21], v231 offset:36928
	ds_read_b128 v[22:25], v231 offset:36944
	ds_read_b128 v[26:29], v231 offset:36960
	ds_read_b128 v[30:33], v231 offset:36976
	v_pk_fma_f32 v[200:201], v[192:193], v[220:221], v[186:187]
	v_pk_fma_f32 v[134:135], v[198:199], v[190:191], v[190:191] neg_lo:[1,0,0] neg_hi:[1,0,0]
	s_nop 0
	v_pk_fma_f32 v[198:199], v[182:183], v[222:223], v[134:135]
	v_mfma_f32_32x32x16_bf16 v[2:17], v[46:49], v[138:141], v[2:17]
	ds_read_b128 v[134:137], v195 offset:16384
	v_add_f32_e32 v182, 1.0, v206
	v_exp_f32_e32 v183, v201
	v_exp_f32_e32 v186, v200
	v_exp_f32_e32 v187, v199
	v_exp_f32_e32 v188, v198
	v_add_f32_e32 v189, 1.0, v207
	v_add_f32_e32 v190, 1.0, v208
	v_add_f32_e32 v191, 1.0, v209
	v_mfma_f32_32x32x16_bf16 v[2:17], v[42:45], v[146:149], v[2:17]
	ds_read_b128 v[138:141], v195 offset:16416
	v_fmac_f32_e32 v182, v182, v183
	v_fmac_f32_e32 v189, v189, v186
	v_fmac_f32_e32 v190, v190, v187
	v_fmac_f32_e32 v191, v191, v188
	v_mfma_f32_32x32x16_bf16 v[2:17], v[38:41], v[150:153], v[2:17]
	ds_read_b128 v[146:149], v195 offset:16448
	v_rcp_f32_e32 v182, v182
	v_rcp_f32_e32 v189, v189
	v_rcp_f32_e32 v190, v190
	v_rcp_f32_e32 v191, v191
	v_mfma_f32_32x32x16_bf16 v[2:17], v[34:37], v[178:181], v[2:17]
	ds_read_b128 v[150:153], v195 offset:16480
	v_fma_f32 v182, -v183, v182, v182
	v_fma_f32 v183, -v186, v189, v189
	v_fma_f32 v186, -v187, v190, v190
	v_fma_f32 v187, -v188, v191, v191
	s_waitcnt lgkmcnt(4)
	v_mfma_f32_32x32x16_bf16 v[18:33], v[126:129], v[174:177], v[18:33]
	v_cvt_pk_bf16_f32 v252, v182, v183
	v_cvt_pk_bf16_f32 v253, v186, v187
	v_mfma_f32_32x32x16_bf16 v[18:33], v[122:125], v[170:173], v[18:33]
	s_nop 1
	v_exp_f32_e32 v179, v4
	v_exp_f32_e32 v178, v8
	v_exp_f32_e32 v181, v12
	v_exp_f32_e32 v180, v16
	v_mfma_f32_32x32x16_bf16 v[18:33], v[118:121], v[166:169], v[18:33]
	v_exp_f32_e32 v2, v2
	v_exp_f32_e32 v6, v6
	v_exp_f32_e32 v10, v10
	v_exp_f32_e32 v12, v14
	v_fma_f32 v4, v179, s12, s12
	v_fma_f32 v8, v178, s12, s12
	v_fma_f32 v14, v181, s12, s12
	v_fma_f32 v16, v180, s12, s12
	v_mfma_f32_32x32x16_bf16 v[18:33], v[114:117], v[162:165], v[18:33]
	v_exp_f32_e32 v3, v3
	v_fmac_f32_e32 v4, v2, v4
	v_exp_f32_e32 v2, v7
	v_fmac_f32_e32 v8, v6, v8
	v_exp_f32_e32 v6, v11
	v_exp_f32_e32 v7, v15
	v_fmac_f32_e32 v14, v10, v14
	v_fmac_f32_e32 v16, v12, v16
	v_mfma_f32_32x32x16_bf16 v[18:33], v[110:113], v[158:161], v[18:33]
	v_add_f32_e32 v10, 1.0, v3
	v_rcp_f32_e32 v3, v4
	v_add_f32_e32 v4, 1.0, v2
	v_rcp_f32_e32 v2, v8
	v_rcp_f32_e32 v183, v14
	v_rcp_f32_e32 v182, v16
	v_mfma_f32_32x32x16_bf16 v[18:33], v[106:109], v[154:157], v[18:33]
	v_add_f32_e32 v6, 1.0, v6
	v_add_f32_e32 v7, 1.0, v7
	v_rcp_f32_e32 v187, v10
	v_rcp_f32_e32 v186, v4
	v_exp_f32_e32 v190, v5
	v_exp_f32_e32 v191, v9
	v_mfma_f32_32x32x16_bf16 v[18:33], v[102:105], v[142:145], v[18:33]
	v_rcp_f32_e32 v189, v6
	v_rcp_f32_e32 v188, v7
	v_exp_f32_e32 v192, v13
	v_exp_f32_e32 v193, v17
	v_mfma_f32_32x32x16_bf16 v[18:33], v[98:101], v[130:133], v[18:33]
	v_fma_f32 v178, -v178, v2, v2
	v_fma_f32 v179, -v179, v3, v3
	v_pk_fma_f32 v[206:207], v[186:187], v[216:217], v[178:179]
	s_nop 0
	v_pk_fma_f32 v[178:179], v[180:181], v[182:183], v[182:183] neg_lo:[1,0,0] neg_hi:[1,0,0]
	s_nop 0
	v_pk_fma_f32 v[208:209], v[188:189], v[218:219], v[178:179]
	s_waitcnt lgkmcnt(0)
	v_mfma_f32_32x32x16_bf16 v[18:33], v[94:97], v[134:137], v[18:33]
	v_add_f32_e32 v178, 1.0, v190
	v_exp_f32_e32 v179, v207
	v_add_f32_e32 v180, 1.0, v191
	v_exp_f32_e32 v181, v206
	v_exp_f32_e32 v182, v209
	v_exp_f32_e32 v183, v208
	v_add_f32_e32 v184, 1.0, v192
	v_add_f32_e32 v185, 1.0, v193
	v_mfma_f32_32x32x16_bf16 v[18:33], v[90:93], v[138:141], v[18:33]
	v_fmac_f32_e32 v178, v178, v179
	v_fmac_f32_e32 v180, v180, v181
	v_fmac_f32_e32 v184, v184, v182
	v_fmac_f32_e32 v185, v185, v183
	v_mfma_f32_32x32x16_bf16 v[18:33], v[86:89], v[146:149], v[18:33]
	v_rcp_f32_e32 v178, v178
	v_rcp_f32_e32 v180, v180
	v_rcp_f32_e32 v184, v184
	v_rcp_f32_e32 v185, v185
	v_mfma_f32_32x32x16_bf16 v[18:33], v[82:85], v[150:153], v[18:33]
	v_fma_f32 v178, -v179, v178, v178
	v_fma_f32 v179, -v181, v180, v180
	v_fma_f32 v180, -v182, v184, v184
	v_fma_f32 v181, -v183, v185, v185
	v_cvt_pk_bf16_f32 v254, v178, v179
	v_cvt_pk_bf16_f32 v255, v180, v181
	ds_write_b128 v211, v[252:255] offset:8192
	s_waitcnt lgkmcnt(0)
	s_barrier
	s_add_i32 s1, s1, 2
	s_cmp_gt_u32 s1, 16
	v_add_u32_e32 v232, 0x200, v232
	s_cbranch_scc1 .LBB1_30
.LBB1_14:
	v_mfma_f32_32x32x16_bf16 v[2:17], v[78:81], v[174:177], v[236:251]
	v_add_u32_e32 v192, v230, v229
	ds_read2_b32 v[228:229], v232 offset1:32
	ds_read_b128 v[194:197], v210 offset:8192
	v_mfma_f32_32x32x16_bf16 v[2:17], v[74:77], v[170:173], v[2:17]
	ds_read_b128 v[178:181], v210 offset:9216
	v_exp_f32_e32 v187, v20
	v_exp_f32_e32 v186, v24
	v_exp_f32_e32 v189, v28
	v_exp_f32_e32 v188, v32
	v_mfma_f32_32x32x16_bf16 v[2:17], v[70:73], v[166:169], v[2:17]
	ds_read_b128 v[170:173], v210 offset:10240
	v_exp_f32_e32 v18, v18
	v_exp_f32_e32 v22, v22
	v_exp_f32_e32 v24, v26
	v_exp_f32_e32 v26, v30
	v_fma_f32 v20, v187, s12, s12
	v_fma_f32 v28, v186, s12, s12
	v_fma_f32 v30, v189, s12, s12
	v_fma_f32 v32, v188, s12, s12
	v_mfma_f32_32x32x16_bf16 v[2:17], v[66:69], v[162:165], v[2:17]
	ds_read_b128 v[166:169], v210 offset:11264
	v_exp_f32_e32 v19, v19
	v_exp_f32_e32 v23, v23
	v_exp_f32_e32 v27, v27
	v_exp_f32_e32 v31, v31
	v_fmac_f32_e32 v20, v18, v20
	v_fmac_f32_e32 v28, v22, v28
	v_fmac_f32_e32 v30, v24, v30
	v_fmac_f32_e32 v32, v26, v32
	v_mfma_f32_32x32x16_bf16 v[2:17], v[62:65], v[158:161], v[2:17]
	ds_read_b128 v[162:165], v210 offset:12288
	v_add_f32_e32 v22, 1.0, v19
	v_rcp_f32_e32 v19, v20
	v_rcp_f32_e32 v18, v28
	v_rcp_f32_e32 v191, v30
	v_rcp_f32_e32 v190, v32
	v_add_f32_e32 v20, 1.0, v23
	v_mfma_f32_32x32x16_bf16 v[2:17], v[58:61], v[154:157], v[2:17]
	ds_read_b128 v[174:177], v210 offset:13312
	v_rcp_f32_e32 v159, v22
	v_rcp_f32_e32 v158, v20
	v_exp_f32_e32 v160, v21
	v_exp_f32_e32 v161, v25
	v_add_f32_e32 v23, 1.0, v27
	v_add_f32_e32 v20, 1.0, v31
	v_mfma_f32_32x32x16_bf16 v[2:17], v[54:57], v[142:145], v[2:17]
	ds_read_b128 v[182:185], v210 offset:14336
	v_rcp_f32_e32 v155, v23
	v_rcp_f32_e32 v154, v20
	v_exp_f32_e32 v193, v29
	v_exp_f32_e32 v217, v33
	v_mfma_f32_32x32x16_bf16 v[2:17], v[50:53], v[130:133], v[2:17]
	ds_read_b128 v[142:145], v210 offset:15360
	v_fma_f32 v156, -v186, v18, v18
	v_fma_f32 v157, -v187, v19, v19
	ds_read_b128 v[18:21], v231 offset:36928
	ds_read_b128 v[22:25], v231 offset:36944
	ds_read_b128 v[26:29], v231 offset:36960
	ds_read_b128 v[30:33], v231 offset:36976
	v_pk_fma_f32 v[214:215], v[158:159], v[214:215], v[156:157]
	v_pk_fma_f32 v[130:131], v[188:189], v[190:191], v[190:191] neg_lo:[1,0,0] neg_hi:[1,0,0]
	s_nop 0
	v_pk_fma_f32 v[212:213], v[154:155], v[212:213], v[130:131]
	v_mfma_f32_32x32x16_bf16 v[2:17], v[46:49], v[134:137], v[2:17]
	ds_read_b128 v[154:157], v192 offset:16384
	v_add_f32_e32 v130, 1.0, v160
	v_exp_f32_e32 v131, v215
	v_exp_f32_e32 v132, v214
	v_exp_f32_e32 v133, v213
	v_exp_f32_e32 v220, v212
	v_add_f32_e32 v134, 1.0, v161
	v_add_f32_e32 v135, 1.0, v193
	v_add_f32_e32 v136, 1.0, v217
	v_mfma_f32_32x32x16_bf16 v[2:17], v[42:45], v[138:141], v[2:17]
	ds_read_b128 v[158:161], v192 offset:16416
	v_fmac_f32_e32 v130, v130, v131
	v_fmac_f32_e32 v134, v134, v132
	v_fmac_f32_e32 v135, v135, v133
	v_fmac_f32_e32 v136, v136, v220
	v_mfma_f32_32x32x16_bf16 v[2:17], v[38:41], v[146:149], v[2:17]
	ds_read_b128 v[186:189], v192 offset:16448
	v_rcp_f32_e32 v130, v130
	v_rcp_f32_e32 v134, v134
	v_rcp_f32_e32 v135, v135
	v_rcp_f32_e32 v136, v136
	v_mfma_f32_32x32x16_bf16 v[2:17], v[34:37], v[150:153], v[2:17]
	ds_read_b128 v[190:193], v192 offset:16480
	v_fma_f32 v130, -v131, v130, v130
	v_fma_f32 v131, -v132, v134, v134
	v_fma_f32 v132, -v133, v135, v135
	v_fma_f32 v133, -v220, v136, v136
	s_waitcnt lgkmcnt(4)
	v_mfma_f32_32x32x16_bf16 v[18:33], v[126:129], v[194:197], v[18:33]
	v_cvt_pk_bf16_f32 v252, v130, v131
	v_cvt_pk_bf16_f32 v253, v132, v133
	v_mfma_f32_32x32x16_bf16 v[18:33], v[122:125], v[178:181], v[18:33]
	s_nop 1
	v_exp_f32_e32 v131, v4
	v_exp_f32_e32 v130, v8
	v_exp_f32_e32 v133, v12
	v_exp_f32_e32 v132, v16
	v_mfma_f32_32x32x16_bf16 v[18:33], v[118:121], v[170:173], v[18:33]
	v_exp_f32_e32 v2, v2
	v_exp_f32_e32 v6, v6
	v_exp_f32_e32 v10, v10
	v_exp_f32_e32 v12, v14
	v_fma_f32 v4, v131, s12, s12
	v_fma_f32 v8, v130, s12, s12
	v_fma_f32 v14, v133, s12, s12
	v_fma_f32 v16, v132, s12, s12
	v_mfma_f32_32x32x16_bf16 v[18:33], v[114:117], v[166:169], v[18:33]
	v_exp_f32_e32 v3, v3
	v_fmac_f32_e32 v4, v2, v4
	v_exp_f32_e32 v2, v7
	v_fmac_f32_e32 v8, v6, v8
	v_exp_f32_e32 v6, v11
	v_exp_f32_e32 v7, v15
	v_fmac_f32_e32 v14, v10, v14
	v_fmac_f32_e32 v16, v12, v16
	v_mfma_f32_32x32x16_bf16 v[18:33], v[110:113], v[162:165], v[18:33]
	v_add_f32_e32 v10, 1.0, v3
	v_rcp_f32_e32 v3, v4
	v_add_f32_e32 v4, 1.0, v2
	v_rcp_f32_e32 v2, v8
	v_rcp_f32_e32 v135, v14
	v_rcp_f32_e32 v134, v16
	v_mfma_f32_32x32x16_bf16 v[18:33], v[106:109], v[174:177], v[18:33]
	v_add_f32_e32 v6, 1.0, v6
	v_add_f32_e32 v7, 1.0, v7
	v_rcp_f32_e32 v137, v10
	v_rcp_f32_e32 v136, v4
	v_exp_f32_e32 v140, v5
	v_exp_f32_e32 v141, v9
	v_mfma_f32_32x32x16_bf16 v[18:33], v[102:105], v[182:185], v[18:33]
	v_rcp_f32_e32 v139, v6
	v_rcp_f32_e32 v138, v7
	v_exp_f32_e32 v146, v13
	v_exp_f32_e32 v147, v17
	v_mfma_f32_32x32x16_bf16 v[18:33], v[98:101], v[142:145], v[18:33]
	v_fma_f32 v130, -v130, v2, v2
	v_fma_f32 v131, -v131, v3, v3
	v_pk_fma_f32 v[224:225], v[136:137], v[204:205], v[130:131]
	s_nop 0
	v_pk_fma_f32 v[130:131], v[132:133], v[134:135], v[134:135] neg_lo:[1,0,0] neg_hi:[1,0,0]
	s_nop 0
	v_pk_fma_f32 v[226:227], v[138:139], v[202:203], v[130:131]
	s_waitcnt lgkmcnt(0)
	v_mfma_f32_32x32x16_bf16 v[18:33], v[94:97], v[154:157], v[18:33]
	v_add_f32_e32 v130, 1.0, v140
	v_exp_f32_e32 v131, v225
	v_add_f32_e32 v132, 1.0, v141
	v_exp_f32_e32 v133, v224
	v_exp_f32_e32 v134, v227
	v_exp_f32_e32 v135, v226
	v_add_f32_e32 v136, 1.0, v146
	v_add_f32_e32 v137, 1.0, v147
	v_mfma_f32_32x32x16_bf16 v[18:33], v[90:93], v[158:161], v[18:33]
	v_fmac_f32_e32 v130, v130, v131
	v_fmac_f32_e32 v132, v132, v133
	v_fmac_f32_e32 v136, v136, v134
	v_fmac_f32_e32 v137, v137, v135
	v_mfma_f32_32x32x16_bf16 v[18:33], v[86:89], v[186:189], v[18:33]
	v_rcp_f32_e32 v130, v130
	v_rcp_f32_e32 v132, v132
	v_rcp_f32_e32 v136, v136
	v_rcp_f32_e32 v137, v137
	v_mfma_f32_32x32x16_bf16 v[18:33], v[82:85], v[190:193], v[18:33]
	v_fma_f32 v130, -v131, v130, v130
	v_fma_f32 v131, -v133, v132, v132
	v_fma_f32 v132, -v134, v136, v136
	v_fma_f32 v133, -v135, v137, v137
	v_cvt_pk_bf16_f32 v254, v130, v131
	v_cvt_pk_bf16_f32 v255, v132, v133
	ds_write_b128 v211, v[252:255] offset:0
	s_waitcnt lgkmcnt(0)
	s_barrier
	v_mfma_f32_32x32x16_bf16 v[2:17], v[78:81], v[194:197], v[236:251]
	ds_read_b128 v[202:205], v210
	v_add_u32_e32 v216, v230, v228
	v_mfma_f32_32x32x16_bf16 v[2:17], v[74:77], v[178:181], v[2:17]
	ds_read_b128 v[194:197], v210 offset:1024
	v_exp_f32_e32 v147, v20
	v_exp_f32_e32 v146, v24
	v_exp_f32_e32 v149, v28
	v_exp_f32_e32 v148, v32
	v_mfma_f32_32x32x16_bf16 v[2:17], v[70:73], v[170:173], v[2:17]
	ds_read_b128 v[138:141], v210 offset:2048
	v_exp_f32_e32 v18, v18
	v_exp_f32_e32 v22, v22
	v_exp_f32_e32 v24, v26
	v_exp_f32_e32 v26, v30
	v_fma_f32 v20, v147, s12, s12
	v_fma_f32 v28, v146, s12, s12
	v_fma_f32 v30, v149, s12, s12
	v_fma_f32 v32, v148, s12, s12
	v_mfma_f32_32x32x16_bf16 v[2:17], v[66:69], v[166:169], v[2:17]
	ds_read_b128 v[134:137], v210 offset:3072
	v_exp_f32_e32 v19, v19
	v_exp_f32_e32 v23, v23
	v_exp_f32_e32 v27, v27
	v_exp_f32_e32 v31, v31
	v_fmac_f32_e32 v20, v18, v20
	v_fmac_f32_e32 v28, v22, v28
	v_fmac_f32_e32 v30, v24, v30
	v_fmac_f32_e32 v32, v26, v32
	v_mfma_f32_32x32x16_bf16 v[2:17], v[62:65], v[162:165], v[2:17]
	ds_read_b128 v[166:169], v210 offset:4096
	v_add_f32_e32 v22, 1.0, v19
	v_rcp_f32_e32 v19, v20
	v_rcp_f32_e32 v18, v28
	v_rcp_f32_e32 v151, v30
	v_rcp_f32_e32 v150, v32
	v_add_f32_e32 v20, 1.0, v23
	v_mfma_f32_32x32x16_bf16 v[2:17], v[58:61], v[174:177], v[2:17]
	ds_read_b128 v[162:165], v210 offset:5120
	v_rcp_f32_e32 v153, v22
	v_rcp_f32_e32 v152, v20
	v_add_f32_e32 v23, 1.0, v27
	v_add_f32_e32 v20, 1.0, v31
	v_exp_f32_e32 v180, v21
	v_exp_f32_e32 v181, v25
	v_mfma_f32_32x32x16_bf16 v[2:17], v[54:57], v[182:185], v[2:17]
	ds_read_b128 v[170:173], v210 offset:6144
	v_rcp_f32_e32 v175, v23
	v_rcp_f32_e32 v174, v20
	v_exp_f32_e32 v176, v29
	v_exp_f32_e32 v177, v33
	v_mfma_f32_32x32x16_bf16 v[2:17], v[50:53], v[142:145], v[2:17]
	ds_read_b128 v[130:133], v210 offset:7168
	v_fma_f32 v146, -v146, v18, v18
	v_fma_f32 v147, -v147, v19, v19
	ds_read_b128 v[18:21], v231 offset:36928
	ds_read_b128 v[22:25], v231 offset:36944
	ds_read_b128 v[26:29], v231 offset:36960
	ds_read_b128 v[30:33], v231 offset:36976
	v_pk_fma_f32 v[220:221], v[152:153], v[200:201], v[146:147]
	v_pk_fma_f32 v[142:143], v[148:149], v[150:151], v[150:151] neg_lo:[1,0,0] neg_hi:[1,0,0]
	s_nop 0
	v_pk_fma_f32 v[222:223], v[174:175], v[198:199], v[142:143]
	v_mfma_f32_32x32x16_bf16 v[2:17], v[46:49], v[154:157], v[2:17]
	ds_read_b128 v[146:149], v216 offset:16384
	v_add_f32_e32 v142, 1.0, v180
	v_exp_f32_e32 v143, v221
	v_exp_f32_e32 v144, v220
	v_exp_f32_e32 v145, v223
	v_exp_f32_e32 v180, v222
	v_add_f32_e32 v154, 1.0, v181
	v_add_f32_e32 v155, 1.0, v176
	v_add_f32_e32 v156, 1.0, v177
	v_mfma_f32_32x32x16_bf16 v[2:17], v[42:45], v[158:161], v[2:17]
	ds_read_b128 v[150:153], v216 offset:16416
	v_fmac_f32_e32 v142, v142, v143
	v_fmac_f32_e32 v154, v154, v144
	v_fmac_f32_e32 v155, v155, v145
	v_fmac_f32_e32 v156, v156, v180
	v_mfma_f32_32x32x16_bf16 v[2:17], v[38:41], v[186:189], v[2:17]
	ds_read_b128 v[174:177], v216 offset:16448
	v_rcp_f32_e32 v142, v142
	v_rcp_f32_e32 v154, v154
	v_rcp_f32_e32 v155, v155
	v_rcp_f32_e32 v156, v156
	v_mfma_f32_32x32x16_bf16 v[2:17], v[34:37], v[190:193], v[2:17]
	ds_read_b128 v[198:201], v216 offset:16480
	v_fma_f32 v142, -v143, v142, v142
	v_fma_f32 v143, -v144, v154, v154
	v_fma_f32 v144, -v145, v155, v155
	v_fma_f32 v145, -v180, v156, v156
	s_waitcnt lgkmcnt(4)
	v_mfma_f32_32x32x16_bf16 v[18:33], v[126:129], v[202:205], v[18:33]
	v_cvt_pk_bf16_f32 v252, v142, v143
	v_cvt_pk_bf16_f32 v253, v144, v145
	v_mfma_f32_32x32x16_bf16 v[18:33], v[122:125], v[194:197], v[18:33]
	s_nop 1
	v_exp_f32_e32 v143, v4
	v_exp_f32_e32 v142, v8
	v_exp_f32_e32 v145, v12
	v_exp_f32_e32 v144, v16
	v_mfma_f32_32x32x16_bf16 v[18:33], v[118:121], v[138:141], v[18:33]
	v_exp_f32_e32 v2, v2
	v_exp_f32_e32 v6, v6
	v_exp_f32_e32 v10, v10
	v_exp_f32_e32 v12, v14
	v_fma_f32 v4, v143, s12, s12
	v_fma_f32 v8, v142, s12, s12
	v_fma_f32 v14, v145, s12, s12
	v_fma_f32 v16, v144, s12, s12
	v_mfma_f32_32x32x16_bf16 v[18:33], v[114:117], v[134:137], v[18:33]
	v_exp_f32_e32 v3, v3
	v_fmac_f32_e32 v4, v2, v4
	v_exp_f32_e32 v2, v7
	v_fmac_f32_e32 v8, v6, v8
	v_exp_f32_e32 v6, v11
	v_exp_f32_e32 v7, v15
	v_fmac_f32_e32 v14, v10, v14
	v_fmac_f32_e32 v16, v12, v16
	v_mfma_f32_32x32x16_bf16 v[18:33], v[110:113], v[166:169], v[18:33]
	v_add_f32_e32 v10, 1.0, v3
	v_rcp_f32_e32 v3, v4
	v_add_f32_e32 v4, 1.0, v2
	v_rcp_f32_e32 v2, v8
	v_rcp_f32_e32 v155, v14
	v_rcp_f32_e32 v154, v16
	v_mfma_f32_32x32x16_bf16 v[18:33], v[106:109], v[162:165], v[18:33]
	v_add_f32_e32 v6, 1.0, v6
	v_add_f32_e32 v7, 1.0, v7
	v_rcp_f32_e32 v157, v10
	v_rcp_f32_e32 v156, v4
	v_exp_f32_e32 v160, v5
	v_exp_f32_e32 v161, v9
	v_mfma_f32_32x32x16_bf16 v[18:33], v[102:105], v[170:173], v[18:33]
	v_rcp_f32_e32 v159, v6
	v_rcp_f32_e32 v158, v7
	v_exp_f32_e32 v180, v13
	v_exp_f32_e32 v181, v17
	v_mfma_f32_32x32x16_bf16 v[18:33], v[98:101], v[130:133], v[18:33]
	v_fma_f32 v142, -v142, v2, v2
	v_fma_f32 v143, -v143, v3, v3
	v_pk_fma_f32 v[216:217], v[156:157], v[206:207], v[142:143]
	s_nop 0
	v_pk_fma_f32 v[142:143], v[144:145], v[154:155], v[154:155] neg_lo:[1,0,0] neg_hi:[1,0,0]
	s_nop 0
	v_pk_fma_f32 v[218:219], v[158:159], v[208:209], v[142:143]
	s_waitcnt lgkmcnt(0)
	v_mfma_f32_32x32x16_bf16 v[18:33], v[94:97], v[146:149], v[18:33]
	v_add_f32_e32 v142, 1.0, v160
	v_exp_f32_e32 v143, v217
	v_add_f32_e32 v144, 1.0, v161
	v_exp_f32_e32 v145, v216
	v_exp_f32_e32 v154, v219
	v_exp_f32_e32 v155, v218
	v_add_f32_e32 v156, 1.0, v180
	v_add_f32_e32 v157, 1.0, v181
	v_mfma_f32_32x32x16_bf16 v[18:33], v[90:93], v[150:153], v[18:33]
	v_fmac_f32_e32 v142, v142, v143
	v_fmac_f32_e32 v144, v144, v145
	v_fmac_f32_e32 v156, v156, v154
	v_fmac_f32_e32 v157, v157, v155
	v_mfma_f32_32x32x16_bf16 v[18:33], v[86:89], v[174:177], v[18:33]
	v_rcp_f32_e32 v142, v142
	v_rcp_f32_e32 v144, v144
	v_rcp_f32_e32 v156, v156
	v_rcp_f32_e32 v157, v157
	v_mfma_f32_32x32x16_bf16 v[18:33], v[82:85], v[198:201], v[18:33]
	v_fma_f32 v142, -v143, v142, v142
	v_fma_f32 v143, -v145, v144, v144
	v_fma_f32 v144, -v154, v156, v156
	v_fma_f32 v145, -v155, v157, v157
	v_cvt_pk_bf16_f32 v254, v142, v143
	v_cvt_pk_bf16_f32 v255, v144, v145
	ds_write_b128 v211, v[252:255] offset:8192
	s_waitcnt lgkmcnt(0)
	s_barrier
	v_mfma_f32_32x32x16_bf16 v[2:17], v[78:81], v[202:205], v[236:251]
	v_add_u32_e32 v234, v230, v229
	ds_read2_b32 v[228:229], v232 offset0:64 offset1:96
	ds_read_b128 v[206:209], v210 offset:8192
	v_mfma_f32_32x32x16_bf16 v[2:17], v[74:77], v[194:197], v[2:17]
	ds_read_b128 v[190:193], v210 offset:9216
	v_exp_f32_e32 v179, v20
	v_exp_f32_e32 v178, v24
	v_exp_f32_e32 v181, v28
	v_exp_f32_e32 v180, v32
	v_mfma_f32_32x32x16_bf16 v[2:17], v[70:73], v[138:141], v[2:17]
	ds_read_b128 v[158:161], v210 offset:10240
	v_exp_f32_e32 v18, v18
	v_exp_f32_e32 v22, v22
	v_exp_f32_e32 v24, v26
	v_exp_f32_e32 v26, v30
	v_fma_f32 v20, v179, s12, s12
	v_fma_f32 v28, v178, s12, s12
	v_fma_f32 v30, v181, s12, s12
	v_fma_f32 v32, v180, s12, s12
	v_mfma_f32_32x32x16_bf16 v[2:17], v[66:69], v[134:137], v[2:17]
	ds_read_b128 v[142:145], v210 offset:11264
	v_exp_f32_e32 v19, v19
	v_exp_f32_e32 v23, v23
	v_exp_f32_e32 v27, v27
	v_exp_f32_e32 v31, v31
	v_fmac_f32_e32 v20, v18, v20
	v_fmac_f32_e32 v28, v22, v28
	v_fmac_f32_e32 v30, v24, v30
	v_fmac_f32_e32 v32, v26, v32
	v_mfma_f32_32x32x16_bf16 v[2:17], v[62:65], v[166:169], v[2:17]
	ds_read_b128 v[154:157], v210 offset:12288
	v_add_f32_e32 v22, 1.0, v19
	v_rcp_f32_e32 v19, v20
	v_rcp_f32_e32 v18, v28
	v_rcp_f32_e32 v139, v30
	v_rcp_f32_e32 v138, v32
	v_add_f32_e32 v20, 1.0, v23
	v_mfma_f32_32x32x16_bf16 v[2:17], v[58:61], v[162:165], v[2:17]
	ds_read_b128 v[182:185], v210 offset:13312
	v_rcp_f32_e32 v141, v22
	v_rcp_f32_e32 v140, v20
	v_add_f32_e32 v23, 1.0, v27
	v_add_f32_e32 v20, 1.0, v31
	v_exp_f32_e32 v168, v21
	v_exp_f32_e32 v169, v25
	v_mfma_f32_32x32x16_bf16 v[2:17], v[54:57], v[170:173], v[2:17]
	ds_read_b128 v[186:189], v210 offset:14336
	v_rcp_f32_e32 v163, v23
	v_rcp_f32_e32 v162, v20
	v_exp_f32_e32 v194, v29
	v_exp_f32_e32 v195, v33
	v_mfma_f32_32x32x16_bf16 v[2:17], v[50:53], v[130:133], v[2:17]
	ds_read_b128 v[134:137], v210 offset:15360
	v_fma_f32 v166, -v178, v18, v18
	v_fma_f32 v167, -v179, v19, v19
	ds_read_b128 v[18:21], v231 offset:36928
	ds_read_b128 v[22:25], v231 offset:36944
	ds_read_b128 v[26:29], v231 offset:36960
	ds_read_b128 v[30:33], v231 offset:36976
	v_pk_fma_f32 v[214:215], v[140:141], v[214:215], v[166:167]
	v_pk_fma_f32 v[130:131], v[180:181], v[138:139], v[138:139] neg_lo:[1,0,0] neg_hi:[1,0,0]
	s_nop 0
	v_pk_fma_f32 v[212:213], v[162:163], v[212:213], v[130:131]
	v_mfma_f32_32x32x16_bf16 v[2:17], v[46:49], v[146:149], v[2:17]
	ds_read_b128 v[138:141], v234 offset:16384
	v_add_f32_e32 v130, 1.0, v168
	v_exp_f32_e32 v131, v215
	v_exp_f32_e32 v132, v214
	v_exp_f32_e32 v133, v213
	v_exp_f32_e32 v162, v212
	v_add_f32_e32 v163, 1.0, v169
	v_add_f32_e32 v166, 1.0, v194
	v_add_f32_e32 v167, 1.0, v195
	v_mfma_f32_32x32x16_bf16 v[2:17], v[42:45], v[150:153], v[2:17]
	ds_read_b128 v[146:149], v234 offset:16416
	v_fmac_f32_e32 v130, v130, v131
	v_fmac_f32_e32 v163, v163, v132
	v_fmac_f32_e32 v166, v166, v133
	v_fmac_f32_e32 v167, v167, v162
	v_mfma_f32_32x32x16_bf16 v[2:17], v[38:41], v[174:177], v[2:17]
	ds_read_b128 v[150:153], v234 offset:16448
	v_rcp_f32_e32 v130, v130
	v_rcp_f32_e32 v163, v163
	v_rcp_f32_e32 v166, v166
	v_rcp_f32_e32 v167, v167
	v_mfma_f32_32x32x16_bf16 v[2:17], v[34:37], v[198:201], v[2:17]
	ds_read_b128 v[178:181], v234 offset:16480
	v_fma_f32 v130, -v131, v130, v130
	v_fma_f32 v131, -v132, v163, v163
	v_fma_f32 v132, -v133, v166, v166
	v_fma_f32 v133, -v162, v167, v167
	s_waitcnt lgkmcnt(4)
	v_mfma_f32_32x32x16_bf16 v[18:33], v[126:129], v[206:209], v[18:33]
	v_cvt_pk_bf16_f32 v252, v130, v131
	v_cvt_pk_bf16_f32 v253, v132, v133
	v_mfma_f32_32x32x16_bf16 v[18:33], v[122:125], v[190:193], v[18:33]
	s_nop 1
	v_exp_f32_e32 v131, v4
	v_exp_f32_e32 v130, v8
	v_exp_f32_e32 v133, v12
	v_exp_f32_e32 v132, v16
	v_mfma_f32_32x32x16_bf16 v[18:33], v[118:121], v[158:161], v[18:33]
	v_exp_f32_e32 v2, v2
	v_exp_f32_e32 v6, v6
	v_exp_f32_e32 v10, v10
	v_exp_f32_e32 v12, v14
	v_fma_f32 v4, v131, s12, s12
	v_fma_f32 v8, v130, s12, s12
	v_fma_f32 v14, v133, s12, s12
	v_fma_f32 v16, v132, s12, s12
	v_mfma_f32_32x32x16_bf16 v[18:33], v[114:117], v[142:145], v[18:33]
	v_exp_f32_e32 v3, v3
	v_fmac_f32_e32 v4, v2, v4
	v_exp_f32_e32 v2, v7
	v_fmac_f32_e32 v8, v6, v8
	v_exp_f32_e32 v6, v11
	v_exp_f32_e32 v7, v15
	v_fmac_f32_e32 v14, v10, v14
	v_fmac_f32_e32 v16, v12, v16
	v_mfma_f32_32x32x16_bf16 v[18:33], v[110:113], v[154:157], v[18:33]
	v_add_f32_e32 v10, 1.0, v3
	v_rcp_f32_e32 v3, v4
	v_add_f32_e32 v4, 1.0, v2
	v_rcp_f32_e32 v2, v8
	v_rcp_f32_e32 v163, v14
	v_rcp_f32_e32 v162, v16
	v_mfma_f32_32x32x16_bf16 v[18:33], v[106:109], v[182:185], v[18:33]
	v_add_f32_e32 v6, 1.0, v6
	v_add_f32_e32 v7, 1.0, v7
	v_rcp_f32_e32 v167, v10
	v_rcp_f32_e32 v166, v4
	v_exp_f32_e32 v170, v5
	v_exp_f32_e32 v171, v9
	v_mfma_f32_32x32x16_bf16 v[18:33], v[102:105], v[186:189], v[18:33]
	v_rcp_f32_e32 v169, v6
	v_rcp_f32_e32 v168, v7
	v_exp_f32_e32 v172, v13
	v_exp_f32_e32 v173, v17
	v_mfma_f32_32x32x16_bf16 v[18:33], v[98:101], v[134:137], v[18:33]
	v_fma_f32 v130, -v130, v2, v2
	v_fma_f32 v131, -v131, v3, v3
	v_pk_fma_f32 v[204:205], v[166:167], v[224:225], v[130:131]
	s_nop 0
	v_pk_fma_f32 v[130:131], v[132:133], v[162:163], v[162:163] neg_lo:[1,0,0] neg_hi:[1,0,0]
	s_nop 0
	v_pk_fma_f32 v[202:203], v[168:169], v[226:227], v[130:131]
	s_waitcnt lgkmcnt(0)
	v_mfma_f32_32x32x16_bf16 v[18:33], v[94:97], v[138:141], v[18:33]
	v_add_f32_e32 v130, 1.0, v170
	v_exp_f32_e32 v131, v205
	v_add_f32_e32 v132, 1.0, v171
	v_exp_f32_e32 v133, v204
	v_exp_f32_e32 v162, v203
	v_exp_f32_e32 v163, v202
	v_add_f32_e32 v164, 1.0, v172
	v_add_f32_e32 v165, 1.0, v173
	v_mfma_f32_32x32x16_bf16 v[18:33], v[90:93], v[146:149], v[18:33]
	v_fmac_f32_e32 v130, v130, v131
	v_fmac_f32_e32 v132, v132, v133
	v_fmac_f32_e32 v164, v164, v162
	v_fmac_f32_e32 v165, v165, v163
	v_mfma_f32_32x32x16_bf16 v[18:33], v[86:89], v[150:153], v[18:33]
	v_rcp_f32_e32 v130, v130
	v_rcp_f32_e32 v132, v132
	v_rcp_f32_e32 v164, v164
	v_rcp_f32_e32 v165, v165
	v_mfma_f32_32x32x16_bf16 v[18:33], v[82:85], v[178:181], v[18:33]
	v_fma_f32 v130, -v131, v130, v130
	v_fma_f32 v131, -v133, v132, v132
	v_fma_f32 v132, -v162, v164, v164
	v_fma_f32 v133, -v163, v165, v165
	v_cvt_pk_bf16_f32 v254, v130, v131
	v_cvt_pk_bf16_f32 v255, v132, v133
	ds_write_b128 v211, v[252:255] offset:0
	s_waitcnt lgkmcnt(0)
	s_barrier
	s_branch .LBB1_13
